# baseline (speedup 1.0000x reference)
.LBB3_22:
	v_readlane_b32 s24, v37, 0
	v_readlane_b32 s25, v37, 16
	s_max_i32 s24, s24, s25
	v_readlane_b32 s25, v37, 32
	s_max_i32 s24, s24, s25
	v_readlane_b32 s25, v37, 48
	s_max_i32 s24, s24, s25
	s_cmp_gt_i32 s24, 31
	s_cbranch_scc0 .Ll2_nohub
	s_setprio 3

.LBB3_55:
	s_waitcnt vmcnt(1)
	v_add_f32_e32 v7, v8, v14
	v_add_f32_e32 v7, v13, v7
	v_mul_f32_e32 v14, 0x3e4ccccd, v7
	v_cmp_lt_f32_e32 vcc, 0, v7
	s_nop 1
	v_cndmask_b32_e32 v7, v14, v7, vcc
	s_or_b64 exec, exec, s[6:7]
	v_mov_b32_e32 v14, 0xff800000
	s_and_saveexec_b64 s[6:7], s[4:5]
	s_cbranch_execnz .LBB3_31
	s_branch .LBB3_32
	s_nop 0
	s_nop 0
	s_nop 0
	s_nop 0
	s_nop 0
	s_nop 0
	s_nop 0
	s_nop 0
	s_nop 0
	s_nop 0
	s_nop 0
	s_nop 0
	s_nop 0
	s_nop 0
	s_nop 0
	s_nop 0
	s_nop 0
	s_nop 0
	s_nop 0
	s_nop 0
	s_nop 0
	s_nop 0
	s_nop 0
	s_nop 0
	s_nop 0
	s_nop 0
	s_nop 0
	s_nop 0
	s_nop 0
	s_nop 0
	s_nop 0
	s_nop 0
	s_nop 0
	s_nop 0
	s_nop 0
	s_nop 0
	s_nop 0
	s_nop 0
	s_nop 0
	s_nop 0
	s_nop 0
	s_nop 0
	s_nop 0
	s_nop 0
	s_nop 0
	s_nop 0
	s_nop 0
	s_nop 0
	s_nop 0
	s_nop 0
	s_nop 0
	s_nop 0
	s_nop 0
	s_nop 0
	s_nop 0
	s_nop 0
	s_nop 0
	s_nop 0
	s_nop 0
	s_endpgm
